# baseline (speedup 1.0000x reference)
.Lka_done:
	v_mfma_f32_32x32x16_bf16 a[16:31], v[176:179], v[144:147], a[16:31]
	v_max3_f32 v156, v112, v113, v80
	v_max3_f32 v157, v114, v115, v81
	v_max3_f32 v156, v156, v82, v83
	ds_read_b128 a[224:227], v217 offset:8192
	v_max3_f32 v156, v156, v116, v117
	v_mfma_f32_32x32x16_bf16 a[32:47], v[168:171], v[128:131], a[32:47]
	v_max3_f32 v157, v157, v118, v119
	v_max3_f32 v156, v156, v84, v85
	v_max3_f32 v157, v157, v86, v87
	ds_read_b128 a[228:231], v199 offset:8192
	v_max3_f32 v156, v156, v120, v121
	v_mfma_f32_32x32x16_bf16 a[48:63], v[168:171], v[144:147], a[48:63]
	v_max3_f32 v157, v157, v122, v123
	v_max3_f32 v156, v156, v88, v89
	v_max3_f32 v157, v157, v90, v91
	ds_read_b128 a[232:235], v198 offset:8192
	v_max3_f32 v156, v156, v124, v125
	v_mfma_f32_32x32x16_bf16 a[64:79], v[160:163], v[128:131], a[64:79]
	v_max3_f32 v157, v157, v126, v127
	v_max3_f32 v156, v156, v92, v93
	v_max3_f32 v157, v157, v94, v95
	ds_read_b128 a[236:239], v197 offset:8192
	v_max3_f32 v158, v96, v97, v64
	v_mfma_f32_32x32x16_bf16 a[80:95], v[160:163], v[144:147], a[80:95]
	v_max3_f32 v159, v98, v99, v65
	v_max3_f32 v158, v158, v66, v67
	ds_read_b128 a[240:243], v217 offset:8320
	v_max3_f32 v158, v158, v100, v101
	v_max3_f32 v159, v159, v102, v103
	v_mfma_f32_32x32x16_bf16 a[96:111], v[136:139], v[128:131], a[96:111]
	v_max3_f32 v158, v158, v68, v69
	v_max3_f32 v159, v159, v70, v71
	ds_read_b128 a[244:247], v199 offset:8320
	v_max3_f32 v128, v158, v104, v105
	v_max3_f32 v129, v159, v106, v107
	v_mfma_f32_32x32x16_bf16 a[112:127], v[136:139], v[144:147], a[112:127]
	v_max3_f32 v128, v128, v72, v73
	v_max3_f32 v129, v129, v74, v75
	ds_read_b128 a[248:251], v198 offset:8320
	v_max3_f32 v128, v128, v108, v109
	v_max3_f32 v129, v129, v110, v111
	v_mfma_f32_32x32x16_bf16 a[0:15], v[132:135], v[52:55], a[0:15]
	v_max3_f32 v128, v128, v76, v77
	v_max3_f32 v130, v129, v78, v79
	ds_read_b128 a[252:255], v197 offset:8320
	s_cmp_gt_u32 s27, 4
	s_cbranch_scc1 .Lkb2_done
	s_waitcnt lgkmcnt(8)
	v_pk_add_f32 v[200:201], v[248:249], v[200:201]
	v_pk_add_f32 v[202:203], v[250:251], v[202:203]
	v_pk_add_f32 v[204:205], v[252:253], v[204:205]
	v_pk_add_f32 v[206:207], v[254:255], v[206:207]
	v_cvt_pk_bf16_f32 v248, v248, v249
	v_cvt_pk_bf16_f32 v249, v250, v251
	v_cvt_pk_bf16_f32 v250, v252, v253
	v_cvt_pk_bf16_f32 v251, v254, v255
	v_lshrrev_b32_e32 v252, 1, v208
	buffer_store_dwordx4 v[248:251], v252, s[4:7], s56 offen sc1
	s_add_i32 s56, s56, 0x1000
	s_nop 1
	global_load_dwordx4 v[248:251], v208, s[54:55] nt
	global_load_dwordx4 v[252:255], v208, s[54:55] offset:16 nt
	s_add_u32 s54, s54, 0x2000
	s_addc_u32 s55, s55, 0
	s_mov_b32 m0, s84
	s_nop 0
	buffer_load_dwordx4 v208, s[80:83], s86 offen lds
	s_mov_b32 m0, s85
	s_nop 0
	buffer_load_dwordx4 v208, s[80:83], s86 offen offset:16 lds
	s_add_i32 s86, s86, 0x2000

.Lkc_done:
	v_mfma_f32_32x32x16_bf16 a[16:31], v[172:175], v[144:147], a[16:31]
	v_max3_f32 v156, v112, v113, v48
	v_max3_f32 v157, v114, v115, v49
	v_max3_f32 v156, v156, v50, v51
	ds_read_b128 a[224:227], v218 offset:8192
	v_max3_f32 v156, v156, v116, v117
	v_mfma_f32_32x32x16_bf16 a[32:47], v[164:167], v[128:131], a[32:47]
	v_max3_f32 v157, v157, v118, v119
	v_max3_f32 v156, v156, v52, v53
	v_max3_f32 v157, v157, v54, v55
	ds_read_b128 a[228:231], v219 offset:8192
	v_max3_f32 v156, v156, v120, v121
	v_mfma_f32_32x32x16_bf16 a[48:63], v[164:167], v[144:147], a[48:63]
	v_max3_f32 v157, v157, v122, v123
	v_max3_f32 v156, v156, v56, v57
	v_max3_f32 v157, v157, v58, v59
	ds_read_b128 a[232:235], v220 offset:8192
	v_max3_f32 v156, v156, v124, v125
	v_mfma_f32_32x32x16_bf16 a[64:79], v[160:163], v[128:131], a[64:79]
	v_max3_f32 v157, v157, v126, v127
	v_max3_f32 v156, v156, v60, v61
	v_max3_f32 v157, v157, v62, v63
	ds_read_b128 a[236:239], v221 offset:8192
	v_max3_f32 v158, v96, v97, v32
	v_mfma_f32_32x32x16_bf16 a[80:95], v[160:163], v[144:147], a[80:95]
	v_max3_f32 v159, v98, v99, v33
	v_max3_f32 v158, v158, v34, v35
	ds_read_b128 a[240:243], v218 offset:8320
	v_max3_f32 v158, v158, v100, v101
	v_max3_f32 v159, v159, v102, v103
	v_mfma_f32_32x32x16_bf16 a[96:111], v[136:139], v[128:131], a[96:111]
	v_max3_f32 v158, v158, v36, v37
	v_max3_f32 v159, v159, v38, v39
	ds_read_b128 a[244:247], v219 offset:8320
	v_max3_f32 v128, v158, v104, v105
	v_max3_f32 v129, v159, v106, v107
	v_mfma_f32_32x32x16_bf16 a[112:127], v[136:139], v[144:147], a[112:127]
	v_max3_f32 v128, v128, v40, v41
	v_max3_f32 v129, v129, v42, v43
	ds_read_b128 a[248:251], v220 offset:8320
	v_max3_f32 v128, v128, v108, v109
	v_max3_f32 v129, v129, v110, v111
	v_mfma_f32_32x32x16_bf16 a[0:15], v[132:135], v[84:87], a[0:15]
	v_max3_f32 v128, v128, v44, v45
	v_max3_f32 v130, v129, v46, v47
	ds_read_b128 a[252:255], v221 offset:8320
	s_cmp_gt_u32 s27, 4
	s_cbranch_scc1 .Lkd2_done
	s_waitcnt lgkmcnt(8)
	v_pk_add_f32 v[200:201], v[248:249], v[200:201]
	v_pk_add_f32 v[202:203], v[250:251], v[202:203]
	v_pk_add_f32 v[204:205], v[252:253], v[204:205]
	v_pk_add_f32 v[206:207], v[254:255], v[206:207]
	v_cvt_pk_bf16_f32 v248, v248, v249
	v_cvt_pk_bf16_f32 v249, v250, v251
	v_cvt_pk_bf16_f32 v250, v252, v253
	v_cvt_pk_bf16_f32 v251, v254, v255
	v_lshrrev_b32_e32 v252, 1, v208
	buffer_store_dwordx4 v[248:251], v252, s[4:7], s56 offen sc1
	s_add_i32 s56, s56, 0x1000
	s_nop 1
	global_load_dwordx4 v[248:251], v208, s[54:55] nt
	global_load_dwordx4 v[252:255], v208, s[54:55] offset:16 nt
	s_add_u32 s54, s54, 0x2000
	s_addc_u32 s55, s55, 0
	s_cmp_gt_u32 s27, 2
	s_cbranch_scc1 .Lkd2_done
	s_mov_b32 m0, s84
	s_nop 0
	buffer_load_dwordx4 v208, s[80:83], s86 offen lds
	s_mov_b32 m0, s85
	s_nop 0
	buffer_load_dwordx4 v208, s[80:83], s86 offen offset:16 lds
	s_add_i32 s86, s86, 0x2000
